# N: MoE-down epilogue body regenerated: convert straight from the bias-initialised accumulators (no moves/adds), two alternating pack register sets
# speedup vs baseline: 1.0027x; 1.0027x over previous
; __device__ __forceinline__ unsigned cvt_pk_bf16(float lo, float hi) { unsigned r; asm volatile("v_cvt_pk_bf16_f32 %0, %1, %2" : "=v"(r) : "v"(lo), "v"(hi)); return r; }
;     __device__ __forceinline__ void operator()(const pg8::f32x4 (&acc)[2][2][4][2], const pg8::Unit& u, int wr, int wc, int fr, int fq) const {
;     ...
; #pragma unroll
;         for (int ai = 0; ai < 2; ++ai)
; #pragma unroll
;             for (int m = 0; m < 4; ++m) {
;                 bf16_t* rowp = YS + (size_t)(u.pm + ai * 128 + wr * 64 + m * 16 + fr) * 1024 + col0;
; #pragma unroll
;                 for (int bj = 0; bj < 2; ++bj) {
;                     const f32x4 v0 = acc[ai][bj][m][0] + bv[bj][0], v1 = acc[ai][bj][m][1] + bv[bj][1];
;                     pg8::u32x4 w; w.x = pg8::cvt_pk_bf16(v0[0], v0[1]); w.y = pg8::cvt_pk_bf16(v0[2], v0[3]); w.z = pg8::cvt_pk_bf16(v1[0], v1[1]); w.w = pg8::cvt_pk_bf16(v1[2], v1[3]);
;                     *(pg8::u32x4*)(rowp + bj * 128) = w;
;                 }
;             }
.Ldn_epi_nonext:
	s_mov_b64 s[4:5], -1
	s_andn2_b64 vcc, exec, s[42:43]
	v_add_u32_e32 v106, s6, v1
	v_ashrrev_i32_e32 v107, 31, v106
	v_lshlrev_b64 v[104:105], 11, v[106:107]
	v_lshl_add_u64 v[104:105], s[10:11], 0, v[104:105]
	v_lshl_add_u64 v[104:105], v[104:105], 0, v[158:159]
	v_cvt_pk_bf16_f32 v100, v144, v145
	v_cvt_pk_bf16_f32 v101, v146, v147
	v_cvt_pk_bf16_f32 v102, v140, v141
	v_cvt_pk_bf16_f32 v103, v142, v143
	global_store_dwordx4 v[104:105], v[100:103], off
	v_cvt_pk_bf16_f32 v108, v136, v137
	v_cvt_pk_bf16_f32 v109, v138, v139
	v_cvt_pk_bf16_f32 v110, v132, v133
	v_cvt_pk_bf16_f32 v111, v134, v135
	global_store_dwordx4 v[104:105], v[108:111], off offset:256
	v_add_u32_e32 v106, s6, v162
	v_ashrrev_i32_e32 v107, 31, v106
	v_lshlrev_b64 v[104:105], 11, v[106:107]
	v_lshl_add_u64 v[104:105], s[10:11], 0, v[104:105]
	v_lshl_add_u64 v[104:105], v[104:105], 0, v[158:159]
	v_cvt_pk_bf16_f32 v100, v128, v129
	v_cvt_pk_bf16_f32 v101, v130, v131
	v_cvt_pk_bf16_f32 v102, v124, v125
	v_cvt_pk_bf16_f32 v103, v126, v127
	global_store_dwordx4 v[104:105], v[100:103], off
	v_cvt_pk_bf16_f32 v108, v120, v121
	v_cvt_pk_bf16_f32 v109, v122, v123
	v_cvt_pk_bf16_f32 v110, v116, v117
	v_cvt_pk_bf16_f32 v111, v118, v119
	global_store_dwordx4 v[104:105], v[108:111], off offset:256
	v_add_u32_e32 v106, s6, v163
	v_ashrrev_i32_e32 v107, 31, v106
	v_lshlrev_b64 v[104:105], 11, v[106:107]
	v_lshl_add_u64 v[104:105], s[10:11], 0, v[104:105]
	v_lshl_add_u64 v[104:105], v[104:105], 0, v[158:159]
	v_cvt_pk_bf16_f32 v100, v96, v97
	v_cvt_pk_bf16_f32 v101, v98, v99
	v_cvt_pk_bf16_f32 v102, v92, v93
	v_cvt_pk_bf16_f32 v103, v94, v95
	global_store_dwordx4 v[104:105], v[100:103], off
	v_cvt_pk_bf16_f32 v108, v88, v89
	v_cvt_pk_bf16_f32 v109, v90, v91
	v_cvt_pk_bf16_f32 v110, v84, v85
	v_cvt_pk_bf16_f32 v111, v86, v87
	global_store_dwordx4 v[104:105], v[108:111], off offset:256
	v_add_u32_e32 v106, s6, v164
	v_ashrrev_i32_e32 v107, 31, v106
	v_lshlrev_b64 v[104:105], 11, v[106:107]
	v_lshl_add_u64 v[104:105], s[10:11], 0, v[104:105]
	v_lshl_add_u64 v[104:105], v[104:105], 0, v[158:159]
	v_cvt_pk_bf16_f32 v100, v80, v81
	v_cvt_pk_bf16_f32 v101, v82, v83
	v_cvt_pk_bf16_f32 v102, v76, v77
	v_cvt_pk_bf16_f32 v103, v78, v79
	global_store_dwordx4 v[104:105], v[100:103], off
	v_cvt_pk_bf16_f32 v108, v72, v73
	v_cvt_pk_bf16_f32 v109, v74, v75
	v_cvt_pk_bf16_f32 v110, v68, v69
	v_cvt_pk_bf16_f32 v111, v70, v71
	global_store_dwordx4 v[104:105], v[108:111], off offset:256
	v_add_u32_e32 v106, s6, v165
	v_ashrrev_i32_e32 v107, 31, v106
	v_lshlrev_b64 v[104:105], 11, v[106:107]
	v_lshl_add_u64 v[104:105], s[10:11], 0, v[104:105]
	v_lshl_add_u64 v[104:105], v[104:105], 0, v[158:159]
	v_cvt_pk_bf16_f32 v100, v64, v65
	v_cvt_pk_bf16_f32 v101, v66, v67
	v_cvt_pk_bf16_f32 v102, v60, v61
	v_cvt_pk_bf16_f32 v103, v62, v63
	global_store_dwordx4 v[104:105], v[100:103], off
	v_cvt_pk_bf16_f32 v108, v56, v57
	v_cvt_pk_bf16_f32 v109, v58, v59
	v_cvt_pk_bf16_f32 v110, v48, v49
	v_cvt_pk_bf16_f32 v111, v50, v51
	global_store_dwordx4 v[104:105], v[108:111], off offset:256
	v_add_u32_e32 v106, s6, v166
	v_ashrrev_i32_e32 v107, 31, v106
	v_lshlrev_b64 v[104:105], 11, v[106:107]
	v_lshl_add_u64 v[104:105], s[10:11], 0, v[104:105]
	v_lshl_add_u64 v[104:105], v[104:105], 0, v[158:159]
	v_cvt_pk_bf16_f32 v100, v52, v53
	v_cvt_pk_bf16_f32 v101, v54, v55
	v_cvt_pk_bf16_f32 v102, v44, v45
	v_cvt_pk_bf16_f32 v103, v46, v47
	global_store_dwordx4 v[104:105], v[100:103], off
	v_cvt_pk_bf16_f32 v108, v40, v41
	v_cvt_pk_bf16_f32 v109, v42, v43
	v_cvt_pk_bf16_f32 v110, v32, v33
	v_cvt_pk_bf16_f32 v111, v34, v35
	global_store_dwordx4 v[104:105], v[108:111], off offset:256
	v_add_u32_e32 v106, s6, v167
	v_ashrrev_i32_e32 v107, 31, v106
	v_lshlrev_b64 v[104:105], 11, v[106:107]
	v_lshl_add_u64 v[104:105], s[10:11], 0, v[104:105]
	v_lshl_add_u64 v[104:105], v[104:105], 0, v[158:159]
	v_cvt_pk_bf16_f32 v100, v36, v37
	v_cvt_pk_bf16_f32 v101, v38, v39
	v_cvt_pk_bf16_f32 v102, v28, v29
	v_cvt_pk_bf16_f32 v103, v30, v31
	global_store_dwordx4 v[104:105], v[100:103], off
	v_cvt_pk_bf16_f32 v108, v24, v25
	v_cvt_pk_bf16_f32 v109, v26, v27
	v_cvt_pk_bf16_f32 v110, v16, v17
	v_cvt_pk_bf16_f32 v111, v18, v19
	global_store_dwordx4 v[104:105], v[108:111], off offset:256
	v_add_u32_e32 v106, s6, v168
	v_ashrrev_i32_e32 v107, 31, v106
	v_lshlrev_b64 v[104:105], 11, v[106:107]
	v_lshl_add_u64 v[104:105], s[10:11], 0, v[104:105]
	v_lshl_add_u64 v[104:105], v[104:105], 0, v[158:159]
	v_cvt_pk_bf16_f32 v100, v20, v21
	v_cvt_pk_bf16_f32 v101, v22, v23
	v_cvt_pk_bf16_f32 v102, v12, v13
	v_cvt_pk_bf16_f32 v103, v14, v15
	global_store_dwordx4 v[104:105], v[100:103], off
	v_cvt_pk_bf16_f32 v108, v8, v9
	v_cvt_pk_bf16_f32 v109, v10, v11
	v_cvt_pk_bf16_f32 v110, v4, v5
	v_cvt_pk_bf16_f32 v111, v6, v7
	global_store_dwordx4 v[104:105], v[108:111], off offset:256
	s_cbranch_vccnz .LBB0_1812
	s_branch .LBB0_1811
